# v24 + GLA pre A-section: the 12 fragment reads issued up front with counted lgkmcnt waits per MFMA pair
# baseline (speedup 1.0000x reference)
.LBB0_410:
	s_or_b64 exec, exec, s[2:3]
	v_add_u32_e32 v5, s17, v55
	v_add3_u32 v21, v5, v56, v54
	v_add_u32_e32 v160, 0xe000, v21
	ds_read_u16 v128, v21 offset:57344
	ds_read_u16 v129, v21 offset:57600
	ds_read_u16 v130, v160 offset:16384
	ds_read_u16 v131, v160 offset:16640
	ds_read_u16 v132, v21 offset:57856
	ds_read_u16 v133, v21 offset:58112
	ds_read_u16 v134, v160 offset:16896
	ds_read_u16 v135, v160 offset:17152
	ds_read_u16 v136, v21 offset:61440
	ds_read_u16 v137, v21 offset:61696
	ds_read_u16 v138, v160 offset:20480
	ds_read_u16 v139, v160 offset:20736
	ds_read_u16 v140, v21 offset:61952
	ds_read_u16 v141, v21 offset:62208
	ds_read_u16 v142, v160 offset:20992
	ds_read_u16 v143, v160 offset:21248
	ds_read_u16 v144, v160 offset:8192
	ds_read_u16 v145, v160 offset:8448
	ds_read_u16 v146, v160 offset:24576
	ds_read_u16 v147, v160 offset:24832
	ds_read_u16 v148, v160 offset:8704
	ds_read_u16 v149, v160 offset:8960
	ds_read_u16 v150, v160 offset:25088
	ds_read_u16 v151, v160 offset:25344
	ds_read_u16 v152, v160 offset:12288
	ds_read_u16 v153, v160 offset:12544
	ds_read_u16 v154, v160 offset:28672
	ds_read_u16 v155, v160 offset:28928
	ds_read_u16 v156, v160 offset:12800
	ds_read_u16 v157, v160 offset:13056
	ds_read_u16 v158, v160 offset:29184
	ds_read_u16 v159, v160 offset:29440
	s_and_b32 s2, s95, 3
	s_mul_i32 s2, s2, 17
	s_ashr_i32 s3, s95, 8
	v_exp_f32_e32 v28, v44
	v_exp_f32_e32 v29, v45
	s_add_i32 s2, s2, s3
	s_mulk_i32 s96, 0x44
	s_add_i32 s16, s2, s96
	s_waitcnt lgkmcnt(15)
	v_lshlrev_b32_e32 v33, 16, v129
	v_lshlrev_b32_e32 v32, 16, v128
	s_mov_b32 s2, 0x3db504f3
	v_pk_mul_f32 v[32:33], v[32:33], s[2:3] op_sel_hi:[1,0]
	v_exp_f32_e32 v20, v30
	v_add_u32_e32 v5, 0xe000, v21
	v_rcp_f32_e32 v30, v28
	v_rcp_f32_e32 v31, v29
	v_pk_mul_f32 v[28:29], v[28:29], v[32:33]
	v_exp_f32_e32 v26, v26
	v_cvt_pk_bf16_f32 v36, v28, v29
	v_exp_f32_e32 v27, v27
	v_exp_f32_e32 v24, v24
	v_exp_f32_e32 v25, v25
	s_waitcnt lgkmcnt(15)
	v_lshlrev_b32_e32 v28, 16, v130
	v_lshlrev_b32_e32 v29, 16, v131
	v_pk_mul_f32 v[32:33], v[30:31], v[28:29]
	v_pk_mul_f32 v[30:31], v[20:21], v[30:31] op_sel_hi:[0,1]
	v_cvt_pk_bf16_f32 v32, v32, v33
	v_add_u32_e32 v33, v57, v60
	ds_write_b16 v33, v36
	ds_write_b16_d16_hi v70, v36
	ds_write_b16 v33, v32 offset:16384
	ds_write_b16_d16_hi v70, v32 offset:16384
	v_pk_mul_f32 v[28:29], v[30:31], v[28:29]
	v_exp_f32_e32 v30, v34
	v_cvt_pk_bf16_f32 v28, v28, v29
	v_exp_f32_e32 v31, v35
	v_rcp_f32_e32 v32, v30
	v_exp_f32_e32 v22, v22
	v_exp_f32_e32 v23, v23
	s_waitcnt lgkmcnt(15)
	v_lshlrev_b32_e32 v35, 16, v133
	v_lshlrev_b32_e32 v34, 16, v132
	v_pk_mul_f32 v[34:35], v[34:35], s[2:3] op_sel_hi:[1,0]
	v_rcp_f32_e32 v33, v31
	v_pk_mul_f32 v[30:31], v[30:31], v[34:35]
	v_exp_f32_e32 v18, v18
	v_cvt_pk_bf16_f32 v29, v30, v31
	v_exp_f32_e32 v19, v19
	v_exp_f32_e32 v16, v16
	v_exp_f32_e32 v17, v17
	s_waitcnt lgkmcnt(15)
	v_lshlrev_b32_e32 v30, 16, v134
	v_lshlrev_b32_e32 v31, 16, v135
	v_pk_mul_f32 v[34:35], v[32:33], v[30:31]
	v_pk_mul_f32 v[32:33], v[20:21], v[32:33] op_sel_hi:[0,1]
	v_pk_mul_f32 v[30:31], v[32:33], v[30:31]
	v_cvt_pk_bf16_f32 v34, v34, v35
	ds_write_b16 v71, v29
	ds_write_b16_d16_hi v72, v29
	ds_write_b16 v71, v34 offset:16384
	ds_write_b16_d16_hi v72, v34 offset:16384
	v_cvt_pk_bf16_f32 v29, v30, v31
	ds_write_b64 v73, v[28:29] offset:32768
	v_rcp_f32_e32 v28, v26
	v_rcp_f32_e32 v29, v27
	v_exp_f32_e32 v6, v6
	s_waitcnt lgkmcnt(15)
	v_lshlrev_b32_e32 v30, 16, v136
	v_lshlrev_b32_e32 v31, 16, v137
	v_pk_mul_f32 v[30:31], v[30:31], s[2:3] op_sel_hi:[1,0]
	v_exp_f32_e32 v7, v7
	v_pk_mul_f32 v[26:27], v[26:27], v[30:31]
	s_ashr_i32 s17, s16, 31
	v_cvt_pk_bf16_f32 v32, v26, v27
	s_movk_i32 s10, 0x2000
	s_waitcnt lgkmcnt(15)
	v_lshlrev_b32_e32 v26, 16, v138
	v_lshlrev_b32_e32 v27, 16, v139
	v_pk_mul_f32 v[30:31], v[28:29], v[26:27]
	v_pk_mul_f32 v[28:29], v[20:21], v[28:29] op_sel_hi:[0,1]
	v_cvt_pk_bf16_f32 v30, v30, v31
	ds_write_b16 v74, v32
	ds_write_b16_d16_hi v75, v32
	ds_write_b16 v74, v30 offset:16384
	ds_write_b16_d16_hi v75, v30 offset:16384
	v_pk_mul_f32 v[26:27], v[28:29], v[26:27]
	v_rcp_f32_e32 v28, v24
	v_cvt_pk_bf16_f32 v26, v26, v27
	v_rcp_f32_e32 v29, v25
	s_waitcnt lgkmcnt(15)
	v_lshlrev_b32_e32 v30, 16, v140
	v_lshlrev_b32_e32 v31, 16, v141
	v_pk_mul_f32 v[30:31], v[30:31], s[2:3] op_sel_hi:[1,0]
	s_nop 0
	v_pk_mul_f32 v[24:25], v[24:25], v[30:31]
	s_nop 0
	v_cvt_pk_bf16_f32 v21, v24, v25
	s_waitcnt lgkmcnt(15)
	v_lshlrev_b32_e32 v24, 16, v142
	v_lshlrev_b32_e32 v25, 16, v143
	v_pk_mul_f32 v[30:31], v[28:29], v[24:25]
	v_pk_mul_f32 v[28:29], v[20:21], v[28:29] op_sel_hi:[0,1]
	v_cvt_pk_bf16_f32 v27, v30, v31
	v_pk_mul_f32 v[24:25], v[28:29], v[24:25]
	ds_write_b16 v76, v21
	ds_write_b16_d16_hi v77, v21
	ds_write_b16 v76, v27 offset:16384
	ds_write_b16_d16_hi v77, v27 offset:16384
	v_cvt_pk_bf16_f32 v27, v24, v25
	ds_write_b64 v78, v[26:27] offset:32768
	v_rcp_f32_e32 v24, v22
	v_rcp_f32_e32 v25, v23
	s_waitcnt lgkmcnt(15)
	v_lshlrev_b32_e32 v27, 16, v145
	v_lshlrev_b32_e32 v26, 16, v144
	v_pk_mul_f32 v[26:27], v[26:27], s[2:3] op_sel_hi:[1,0]
	s_nop 0
	v_pk_mul_f32 v[22:23], v[22:23], v[26:27]
	s_nop 0
	v_cvt_pk_bf16_f32 v21, v22, v23
	s_waitcnt lgkmcnt(15)
	v_lshlrev_b32_e32 v22, 16, v146
	v_lshlrev_b32_e32 v23, 16, v147
	v_pk_mul_f32 v[26:27], v[24:25], v[22:23]
	v_pk_mul_f32 v[24:25], v[20:21], v[24:25] op_sel_hi:[0,1]
	v_cvt_pk_bf16_f32 v26, v26, v27
	ds_write_b16 v79, v21
	ds_write_b16_d16_hi v80, v21
	ds_write_b16 v79, v26 offset:16384
	ds_write_b16_d16_hi v80, v26 offset:16384
	v_pk_mul_f32 v[22:23], v[24:25], v[22:23]
	v_rcp_f32_e32 v24, v18
	v_cvt_pk_bf16_f32 v22, v22, v23
	v_rcp_f32_e32 v25, v19
	s_waitcnt lgkmcnt(15)
	v_lshlrev_b32_e32 v26, 16, v148
	v_lshlrev_b32_e32 v27, 16, v149
	v_pk_mul_f32 v[26:27], v[26:27], s[2:3] op_sel_hi:[1,0]
	s_nop 0
	v_pk_mul_f32 v[18:19], v[18:19], v[26:27]
	s_nop 0
	v_cvt_pk_bf16_f32 v21, v18, v19
	s_waitcnt lgkmcnt(15)
	v_lshlrev_b32_e32 v18, 16, v150
	v_lshlrev_b32_e32 v19, 16, v151
	v_pk_mul_f32 v[26:27], v[24:25], v[18:19]
	v_pk_mul_f32 v[24:25], v[20:21], v[24:25] op_sel_hi:[0,1]
	v_cvt_pk_bf16_f32 v23, v26, v27
	v_pk_mul_f32 v[18:19], v[24:25], v[18:19]
	ds_write_b16 v81, v21
	ds_write_b16_d16_hi v82, v21
	ds_write_b16 v81, v23 offset:16384
	ds_write_b16_d16_hi v82, v23 offset:16384
	v_cvt_pk_bf16_f32 v23, v18, v19
	ds_write_b64 v83, v[22:23] offset:32768
	v_rcp_f32_e32 v18, v16
	v_rcp_f32_e32 v19, v17
	s_waitcnt lgkmcnt(15)
	v_lshlrev_b32_e32 v23, 16, v153
	v_lshlrev_b32_e32 v22, 16, v152
	v_pk_mul_f32 v[22:23], v[22:23], s[2:3] op_sel_hi:[1,0]
	s_nop 0
	v_pk_mul_f32 v[16:17], v[16:17], v[22:23]
	s_nop 0
	v_cvt_pk_bf16_f32 v21, v16, v17
	s_waitcnt lgkmcnt(15)
	v_lshlrev_b32_e32 v16, 16, v154
	v_lshlrev_b32_e32 v17, 16, v155
	v_pk_mul_f32 v[22:23], v[18:19], v[16:17]
	v_pk_mul_f32 v[18:19], v[20:21], v[18:19] op_sel_hi:[0,1]
	v_cvt_pk_bf16_f32 v22, v22, v23
	ds_write_b16 v84, v21
	ds_write_b16_d16_hi v85, v21
	ds_write_b16 v84, v22 offset:16384
	ds_write_b16_d16_hi v85, v22 offset:16384
	v_pk_mul_f32 v[16:17], v[18:19], v[16:17]
	v_rcp_f32_e32 v18, v6
	v_cvt_pk_bf16_f32 v16, v16, v17
	v_rcp_f32_e32 v19, v7
	s_waitcnt lgkmcnt(15)
	v_lshlrev_b32_e32 v22, 16, v156
	v_lshlrev_b32_e32 v23, 16, v157
	v_pk_mul_f32 v[22:23], v[22:23], s[2:3] op_sel_hi:[1,0]
	s_lshl_b64 s[2:3], s[16:17], 14
	v_pk_mul_f32 v[6:7], v[6:7], v[22:23]
	s_nop 0
	v_cvt_pk_bf16_f32 v17, v6, v7
	s_waitcnt lgkmcnt(15)
	v_lshlrev_b32_e32 v6, 16, v158
	v_lshlrev_b32_e32 v7, 16, v159
	v_pk_mul_f32 v[22:23], v[18:19], v[6:7]
	v_pk_mul_f32 v[18:19], v[20:21], v[18:19] op_sel_hi:[0,1]
	v_cvt_pk_bf16_f32 v5, v22, v23
	v_pk_mul_f32 v[6:7], v[18:19], v[6:7]
	ds_write_b16 v86, v17
	ds_write_b16_d16_hi v87, v17
	ds_write_b16 v86, v5 offset:16384
	ds_write_b16_d16_hi v87, v5 offset:16384
	v_cvt_pk_bf16_f32 v17, v6, v7
	v_add_u32_e32 v5, v58, v61
	ds_write_b64 v88, v[16:17] offset:32768
	s_waitcnt lgkmcnt(0)
	s_barrier
	ds_read_b128 v[128:131], v5
	v_add_u32_e32 v5, s81, v62
	ds_read_b128 v[132:135], v5 offset:16384
	v_add_u32_e32 v5, s82, v62
	ds_read_b128 v[136:139], v5 offset:16384
	v_add_u32_e32 v5, v58, v63
	ds_read_b128 v[140:143], v5
	v_add_u32_e32 v5, s81, v65
	ds_read_b128 v[144:147], v5 offset:16384
	v_add_u32_e32 v5, s82, v65
	ds_read_b128 v[148:151], v5 offset:16384
	v_add_u32_e32 v5, v58, v66
	ds_read_b128 v[152:155], v5
	v_add_u32_e32 v5, s81, v67
	ds_read_b128 v[156:159], v5 offset:16384
	v_add_u32_e32 v5, s82, v67
	ds_read_b128 v[160:163], v5 offset:16384
	v_add_u32_e32 v5, v58, v68
	ds_read_b128 v[164:167], v5
	v_add_u32_e32 v5, s81, v69
	ds_read_b128 v[168:171], v5 offset:16384
	v_add_u32_e32 v5, s82, v69
	ds_read_b128 v[172:175], v5 offset:16384
	s_waitcnt lgkmcnt(10)
	v_mfma_f32_16x16x32_bf16 v[20:23], v[132:135], v[128:131], 0
	v_cndmask_b32_e64 v6, 0, 1, s[26:27]
	v_cndmask_b32_e64 v7, 0, 1, s[18:19]
	s_waitcnt lgkmcnt(9)
	v_mfma_f32_16x16x32_bf16 v[16:19], v[136:139], v[128:131], 0
	s_waitcnt lgkmcnt(7)
	v_mfma_f32_16x16x32_bf16 v[20:23], v[144:147], v[140:143], v[20:23]
	s_waitcnt lgkmcnt(6)
	v_mfma_f32_16x16x32_bf16 v[16:19], v[148:151], v[140:143], v[16:19]
	s_waitcnt lgkmcnt(4)
	v_mfma_f32_16x16x32_bf16 v[20:23], v[156:159], v[152:155], v[20:23]
	s_waitcnt lgkmcnt(3)
	v_mfma_f32_16x16x32_bf16 v[16:19], v[160:163], v[152:155], v[16:19]
	s_waitcnt lgkmcnt(1)
	v_mfma_f32_16x16x32_bf16 v[20:23], v[168:171], v[164:167], v[20:23]
	s_nop 0
	v_cndmask_b32_e64 v5, 0, 1, s[74:75]
	v_cndmask_b32_e64 v5, v6, v5, s[72:73]
	v_cndmask_b32_e64 v6, 0, 1, s[20:21]
	v_and_b32_e32 v5, 1, v5
	v_cndmask_b32_e64 v6, v7, v6, s[72:73]
	v_cmp_eq_u32_e32 vcc, 1, v5
	v_and_b32_e32 v6, 1, v6
	v_cndmask_b32_e64 v7, 0, 1, s[24:25]
	v_cndmask_b32_e32 v5, 0, v20, vcc
	v_cmp_eq_u32_e32 vcc, 1, v6
	v_cndmask_b32_e64 v20, 0, 1, s[22:23]
	v_cndmask_b32_e64 v7, v20, v7, s[72:73]
	v_cndmask_b32_e32 v6, 0, v21, vcc
	v_cndmask_b32_e64 v20, 0, 1, s[54:55]
	v_cndmask_b32_e64 v21, 0, 1, s[52:53]
	v_and_b32_e32 v7, 1, v7
	v_cndmask_b32_e64 v20, v21, v20, s[72:73]
	v_cmp_eq_u32_e32 vcc, 1, v7
	v_and_b32_e32 v20, 1, v20
	v_cvt_pk_bf16_f32 v6, v5, v6
	v_cndmask_b32_e32 v7, 0, v22, vcc
	v_cmp_eq_u32_e32 vcc, 1, v20
	s_waitcnt lgkmcnt(0)
	v_mfma_f32_16x16x32_bf16 v[16:19], v[172:175], v[164:167], v[16:19]
	v_cndmask_b32_e64 v5, 0, 1, s[58:59]
	v_cndmask_b32_e32 v20, 0, v23, vcc
	v_cvt_pk_bf16_f32 v7, v7, v20
	ds_write_b64 v89, v[6:7] offset:49152
	v_cndmask_b32_e64 v6, 0, 1, s[56:57]
	v_cndmask_b32_e64 v5, v6, v5, s[72:73]
	v_cndmask_b32_e64 v6, 0, 1, s[62:63]
	v_cndmask_b32_e64 v7, 0, 1, s[60:61]
	v_and_b32_e32 v5, 1, v5
	v_cndmask_b32_e64 v6, v7, v6, s[72:73]
	v_cmp_eq_u32_e32 vcc, 1, v5
	v_and_b32_e32 v6, 1, v6
	v_cndmask_b32_e64 v7, 0, 1, s[66:67]
	v_cndmask_b32_e32 v5, 0, v16, vcc
	v_cmp_eq_u32_e32 vcc, 1, v6
	v_cndmask_b32_e64 v16, 0, 1, s[64:65]
	v_cndmask_b32_e64 v7, v16, v7, s[72:73]
	v_cndmask_b32_e32 v6, 0, v17, vcc
	v_cndmask_b32_e64 v16, 0, 1, s[70:71]
	v_cndmask_b32_e64 v17, 0, 1, s[68:69]
	v_and_b32_e32 v7, 1, v7
	v_cndmask_b32_e64 v16, v17, v16, s[72:73]
	v_cmp_eq_u32_e32 vcc, 1, v7
	v_and_b32_e32 v16, 1, v16
	v_cvt_pk_bf16_f32 v6, v5, v6
	v_cndmask_b32_e32 v7, 0, v18, vcc
	v_cmp_eq_u32_e32 vcc, 1, v16
	v_add_u32_e32 v5, 0, v59
	s_add_u32 s72, s86, s2
	v_cndmask_b32_e32 v16, 0, v19, vcc
	v_cvt_pk_bf16_f32 v7, v7, v16
	ds_write_b64 v90, v[6:7] offset:49152
	s_waitcnt lgkmcnt(0)
	s_barrier
	ds_read_b128 v[128:131], v5
	ds_read_b128 v[132:135], v91
	ds_read_b128 v[136:139], v5 offset:32768
	ds_read_b128 v[140:143], v91 offset:32768
	ds_read_b128 v[144:147], v5 offset:49152
	s_addc_u32 s73, s87, s3
	v_lshlrev_b64 v[6:7], 4, v[12:13]
	v_lshl_add_u64 v[20:21], s[72:73], 0, v[6:7]
	s_add_u32 s96, s88, s2
	s_waitcnt lgkmcnt(4)
	global_store_dwordx4 v[20:21], v[128:131], off
	v_add_co_u32_e32 v20, vcc, s10, v20
	s_addc_u32 s97, s89, s3
	s_nop 0
	v_addc_co_u32_e32 v21, vcc, 0, v21, vcc
	s_waitcnt lgkmcnt(3)
	global_store_dwordx4 v[20:21], v[132:135], off
	v_lshl_add_u64 v[20:21], s[96:97], 0, v[6:7]
	s_lshl_b64 s[2:3], s[16:17], 13
	s_add_u32 s2, s90, s2
	s_addc_u32 s3, s91, s3
	s_waitcnt lgkmcnt(2)
	global_store_dwordx4 v[20:21], v[136:139], off
	v_add_co_u32_e32 v20, vcc, 0x2000, v20
	v_lshl_add_u64 v[6:7], s[2:3], 0, v[6:7]
	s_nop 0
	v_addc_co_u32_e32 v21, vcc, 0, v21, vcc
	s_waitcnt lgkmcnt(1)
	global_store_dwordx4 v[20:21], v[140:143], off
	s_waitcnt lgkmcnt(0)
	global_store_dwordx4 v[6:7], v[144:147], off
	s_and_saveexec_b64 s[2:3], s[76:77]
	s_cbranch_execz .LBB0_393
	v_add_u32_e32 v5, 0x22000, v5
	ds_read_b128 v[16:19], v5
	s_lshl_b64 s[16:17], s[16:17], 9
	s_add_u32 s16, s92, s16
	s_addc_u32 s17, s93, s17
	v_lshl_add_u64 v[6:7], v[12:13], 4, s[16:17]
	s_waitcnt lgkmcnt(0)
	global_store_dwordx4 v[6:7], v[16:19], off
	s_branch .LBB0_393
